# stack7_nt_cvnt + non-temporal hint on the final phase's x1 / expert-output row loads
# speedup vs baseline: 1.0029x; 1.0021x over previous
; __device__ __forceinline__ void p9_final(const Params& P, int tid, int blk, int G) {
;     const int wave = tid >> 6, lane = tid & 63;
;     const float* mod = (const float*)(P.ws + WS_MOD); const unsigned char* Y2 = P.ws + WS_Y2; const bf16_t* X1 = (const bf16_t*)(P.ws + WS_X1);
;     f32x4 gf[8];
; #pragma unroll
;     for (int i = 0; i < 8; ++i) gf[i] = *(const f32x4*)(P.in[26] + (i * 64 + lane) * 4);
;     int row = blk * 8 + wave;
;     u32x2 xw[8], xwn[8]; unsigned ya[8], yb[8], yan[8], ybn[8];
;     if (row < NTOK) {
; #pragma unroll
;         for (int i = 0; i < 8; ++i) { const int k = (i * 64 + lane) * 4; xw[i] = *(const u32x2*)(X1 + (size_t)row * DM + k); ya[i] = *(const unsigned*)(Y2 + (size_t)(2 * row) * DM + k); yb[i] = *(const unsigned*)(Y2 + (size_t)(2 * row + 1) * DM + k); }
;     }
.LBB0_1456:
	s_cmp_lt_i32 s38, 10
	s_cselect_b64 s[4:5], -1, 0
	s_and_b64 s[0:1], s[4:5], s[0:1]
	s_andn2_b64 vcc, exec, s[0:1]
	s_cbranch_vccnz .LBB0_1462
	v_lshrrev_b32_e32 v1, 6, v0
	s_waitcnt vmcnt(0)
	v_lshl_or_b32 v88, s2, 3, v1
	s_movk_i32 s13, 0x4000
	v_cmp_gt_i32_e32 vcc, s13, v88
	s_and_saveexec_b64 s[0:1], vcc
	s_cbranch_execz .LBB0_1462
	v_lshlrev_b32_e32 v1, 2, v0
	s_waitcnt lgkmcnt(0)
	v_and_b32_e32 v34, 0xfc, v1
	v_lshlrev_b32_e32 v1, 2, v34
	v_or_b32_e32 v48, 0x400, v34
	global_load_dwordx4 v[2:5], v1, s[20:21]
	global_load_dwordx4 v[6:9], v1, s[20:21] offset:1024
	global_load_dwordx4 v[10:13], v1, s[20:21] offset:2048
	global_load_dwordx4 v[14:17], v1, s[20:21] offset:3072
	v_lshlrev_b32_e32 v1, 2, v48
	v_or_b32_e32 v50, 0x500, v34
	v_or_b32_e32 v52, 0x600, v34
	v_or_b32_e32 v54, 0x700, v34
	v_lshlrev_b32_e32 v38, 1, v88
	v_lshlrev_b32_e32 v26, 2, v50
	global_load_dwordx4 v[18:21], v1, s[20:21]
	global_load_dwordx4 v[22:25], v26, s[20:21]
	v_lshlrev_b32_e32 v1, 2, v52
	v_lshlrev_b32_e32 v36, 2, v54
	v_ashrrev_i32_e32 v89, 31, v88
	v_ashrrev_i32_e32 v39, 31, v38
	v_mov_b32_e32 v35, 0
	global_load_dwordx4 v[26:29], v1, s[20:21]
	global_load_dwordx4 v[30:33], v36, s[20:21]
	v_lshlrev_b64 v[36:37], 12, v[88:89]
	v_lshlrev_b64 v[40:41], 11, v[38:39]
	v_or_b32_e32 v38, 1, v38
	s_add_u32 s0, s36, 0x1f41e000
	v_lshl_add_u64 v[36:37], s[36:37], 0, v[36:37]
	v_ashrrev_i32_e32 v39, 31, v38
	v_lshlrev_b32_e32 v42, 1, v34
	v_mov_b32_e32 v43, v35
	s_addc_u32 s1, s37, 0
	v_lshlrev_b64 v[38:39], 11, v[38:39]
	v_lshl_add_u64 v[36:37], v[36:37], 0, v[42:43]
	s_mov_b64 s[6:7], 0x2f69e000
	s_mov_b32 s2, 0x2f69e000
	v_lshl_add_u64 v[40:41], s[0:1], 0, v[40:41]
	v_lshl_add_u64 v[38:39], s[0:1], 0, v[38:39]
	v_lshl_add_u64 v[42:43], v[36:37], 0, s[6:7]
	v_add_co_u32_e32 v36, vcc, s2, v36
	v_lshl_add_u64 v[40:41], v[40:41], 0, v[34:35]
	s_nop 0
	v_addc_co_u32_e32 v37, vcc, 0, v37, vcc
	v_lshl_add_u64 v[38:39], v[38:39], 0, v[34:35]
	global_load_dwordx2 v[84:85], v[42:43], off offset:512 nt
	global_load_dwordx2 v[82:83], v[42:43], off offset:1024 nt
	global_load_dwordx2 v[80:81], v[42:43], off offset:1536 nt
	global_load_dwordx2 v[78:79], v[42:43], off offset:2048 nt
	global_load_dwordx2 v[86:87], v[36:37], off nt
	global_load_dwordx2 v[76:77], v[42:43], off offset:2560 nt
	global_load_dwordx2 v[74:75], v[42:43], off offset:3072 nt
	global_load_dwordx2 v[72:73], v[42:43], off offset:3584 nt
	global_load_dword v49, v[40:41], off nt
	global_load_dword v121, v[40:41], off offset:256 nt
	global_load_dword v51, v[40:41], off offset:512 nt
	global_load_dword v53, v[40:41], off offset:768 nt
	global_load_dword v117, v[40:41], off offset:1024 nt
	global_load_dword v116, v[40:41], off offset:1280 nt
	global_load_dword v114, v[40:41], off offset:1536 nt
	global_load_dword v104, v[40:41], off offset:1792 nt
	global_load_dword v124, v[38:39], off nt
	global_load_dword v123, v[38:39], off offset:256 nt
	global_load_dword v122, v[38:39], off offset:512 nt
	global_load_dword v55, v[38:39], off offset:768 nt
	global_load_dword v119, v[38:39], off offset:1024 nt
	global_load_dword v118, v[38:39], off offset:1280 nt
	global_load_dword v115, v[38:39], off offset:1536 nt
	global_load_dword v113, v[38:39], off offset:1792 nt
	v_mbcnt_lo_u32_b32 v1, -1, 0
	v_mbcnt_hi_u32_b32 v1, -1, v1
	v_and_b32_e32 v37, 64, v1
	v_xor_b32_e32 v36, 1, v1
	v_add_u32_e32 v37, 64, v37
	v_cmp_lt_i32_e32 vcc, v36, v37
	s_lshl_b32 s2, s33, 3
	v_add_u32_e32 v40, s2, v88
	v_cndmask_b32_e32 v36, v1, v36, vcc
	v_lshlrev_b32_e32 v90, 2, v36
	v_xor_b32_e32 v36, 2, v1
	v_cmp_lt_i32_e32 vcc, v36, v37
	v_ashrrev_i32_e32 v41, 31, v40
	v_lshlrev_b32_e32 v38, 1, v40
	v_cndmask_b32_e32 v36, v1, v36, vcc
	v_lshlrev_b32_e32 v91, 2, v36
	v_xor_b32_e32 v36, 4, v1
	v_cmp_lt_i32_e32 vcc, v36, v37
	v_lshlrev_b64 v[56:57], 13, v[88:89]
	v_and_b32_e32 v39, 63, v0
	v_cndmask_b32_e32 v36, v1, v36, vcc
	v_lshlrev_b32_e32 v92, 2, v36
	v_xor_b32_e32 v36, 8, v1
	v_cmp_lt_i32_e32 vcc, v36, v37
	v_lshlrev_b64 v[40:41], 12, v[40:41]
	v_lshl_or_b32 v56, v39, 4, v56
	v_cndmask_b32_e32 v36, v1, v36, vcc
	v_lshlrev_b32_e32 v93, 2, v36
	v_xor_b32_e32 v36, 16, v1
	v_cmp_lt_i32_e32 vcc, v36, v37
	v_lshl_or_b32 v40, v39, 3, v40
	v_or_b32_e32 v42, 0x100, v34
	v_cndmask_b32_e32 v36, v1, v36, vcc
	v_lshlrev_b32_e32 v94, 2, v36
	v_xor_b32_e32 v36, 32, v1
	v_cmp_lt_i32_e32 vcc, v36, v37
	v_or_b32_e32 v44, 0x200, v34
	v_or_b32_e32 v46, 0x300, v34
	v_cndmask_b32_e32 v1, v1, v36, vcc
	v_lshlrev_b32_e32 v95, 2, v1
	v_lshl_add_u64 v[36:37], s[0:1], 0, v[34:35]
	v_lshl_add_u64 v[0:1], s[22:23], 0, v[56:57]
	s_mov_b64 s[0:1], 0x1000
	s_ashr_i32 s3, s2, 31
	v_lshl_add_u64 v[40:41], s[36:37], 0, v[40:41]
	s_lshl_b32 s16, s33, 4
	v_lshl_add_u64 v[0:1], v[0:1], 0, s[0:1]
	s_lshl_b64 s[4:5], s[2:3], 13
	v_lshl_add_u64 v[40:41], v[40:41], 0, s[6:7]
	s_lshl_b64 s[6:7], s[2:3], 12
	s_mov_b64 s[8:9], 0
	s_movk_i32 s3, 0x3fff
	s_mov_b64 s[10:11], 0x490000
	v_lshlrev_b32_e32 v34, 2, v34
	s_mov_b32 s12, 0x3d800000
	v_lshlrev_b32_e32 v42, 2, v42
	v_lshlrev_b32_e32 v44, 2, v44
	v_lshlrev_b32_e32 v46, 2, v46
	v_lshlrev_b32_e32 v48, 2, v48
	v_lshlrev_b32_e32 v50, 2, v50
	v_lshlrev_b32_e32 v52, 2, v52
	v_lshlrev_b32_e32 v54, 2, v54
	v_mov_b32_e32 v96, 0x358637bd
	s_mov_b32 s17, 0x800000
	s_branch .LBB0_1460

; __device__ __forceinline__ void p9_final(const Params& P, int tid, int blk, int G) {
;     ...
;     for (; row < NTOK; row += G * 8) {
;         const int b = row >> 11, rown = row + G * 8;
;         if (rown < NTOK) {
; #pragma unroll
;             for (int i = 0; i < 8; ++i) { const int k = (i * 64 + lane) * 4; xwn[i] = *(const u32x2*)(X1 + (size_t)rown * DM + k); yan[i] = *(const unsigned*)(Y2 + (size_t)(2 * rown) * DM + k); ybn[i] = *(const unsigned*)(Y2 + (size_t)(2 * rown + 1) * DM + k); }
;         }
.LBB0_1460:
	v_add_u32_e32 v120, s2, v88
	v_cmp_gt_i32_e64 s[0:1], s13, v120
	v_cmp_lt_i32_e32 vcc, s3, v120
	s_and_saveexec_b64 s[14:15], s[0:1]
	s_cbranch_execz .LBB0_1459
	v_add_u32_e32 v58, 1, v38
	v_ashrrev_i32_e32 v39, 31, v38
	v_ashrrev_i32_e32 v59, 31, v58
	v_lshlrev_b64 v[56:57], 11, v[38:39]
	v_lshlrev_b64 v[58:59], 11, v[58:59]
	v_lshl_add_u64 v[126:127], v[36:37], 0, v[56:57]
	v_lshl_add_u64 v[128:129], v[36:37], 0, v[58:59]
	global_load_dwordx2 v[56:57], v[40:41], off nt
	global_load_dwordx2 v[58:59], v[40:41], off offset:512 nt
	global_load_dwordx2 v[60:61], v[40:41], off offset:1024 nt
	global_load_dwordx2 v[62:63], v[40:41], off offset:1536 nt
	global_load_dwordx2 v[64:65], v[40:41], off offset:2048 nt
	global_load_dwordx2 v[66:67], v[40:41], off offset:2560 nt
	global_load_dwordx2 v[68:69], v[40:41], off offset:3072 nt
	global_load_dwordx2 v[70:71], v[40:41], off offset:3584 nt
	global_load_dword v103, v[126:127], off nt
	global_load_dword v102, v[126:127], off offset:256 nt
	global_load_dword v101, v[126:127], off offset:512 nt
	global_load_dword v100, v[126:127], off offset:768 nt
	global_load_dword v99, v[126:127], off offset:1024 nt
	global_load_dword v98, v[126:127], off offset:1280 nt
	global_load_dword v97, v[126:127], off offset:1536 nt
	global_load_dword v39, v[126:127], off offset:1792 nt
	global_load_dword v112, v[128:129], off nt
	global_load_dword v111, v[128:129], off offset:256 nt
	global_load_dword v110, v[128:129], off offset:512 nt
	global_load_dword v109, v[128:129], off offset:768 nt
	global_load_dword v108, v[128:129], off offset:1024 nt
	global_load_dword v107, v[128:129], off offset:1280 nt
	global_load_dword v106, v[128:129], off offset:1536 nt
	global_load_dword v105, v[128:129], off offset:1792 nt
	s_branch .LBB0_1459
